# plucker B-tile dedup (3 DMA/tile), DMA issue after fragment reads, QKV epilogue bias preloaded + hand-written staging
# speedup vs baseline: 1.0289x; 1.0289x over previous
_Z12gemm1_kernel6G1Args:
	s_load_dwordx2 s[24:25], s[0:1], 0x8
	s_load_dwordx16 s[8:23], s[0:1], 0x18
	s_ashr_i32 s3, s2, 3
	v_and_b32_e32 v42, 15, v0
	v_bfe_u32 v1, v0, 4, 2
	v_lshrrev_b32_e32 v78, 8, v0
	s_mov_b64 s[4:5], -1
	s_cmp_gt_i32 s3, 23
	v_lshrrev_b32_e32 v44, 4, v0
	v_lshrrev_b32_e32 v43, 1, v0
	v_lshlrev_b32_e32 v79, 4, v0
	s_cbranch_scc0 .LBB1_32
	s_lshl_b32 s4, s2, 8
	s_and_b32 s4, s4, 0x700
	s_lshl_b32 s5, s3, 5
	s_add_i32 s33, s5, s4
	s_addk_i32 s33, 0xfd00
	s_load_dwordx2 s[26:27], s[0:1], 0x10
	s_bfe_u32 s28, s2, 0x10003
	s_and_b32 s39, s33, 0xffffffc0
	s_and_b32 s7, 8, s2
	s_cmp_eq_u32 s28, 0
	s_cselect_b64 s[4:5], -1, 0
	s_cmp_lg_u32 s7, 0
	s_cselect_b64 s[6:7], -1, 0
	s_mul_i32 s28, s28, 0xc0000
	v_lshrrev_b32_e32 v45, 6, v0
	v_sub_u32_e32 v2, 0, v44
	v_xor_b32_e32 v2, v0, v2
	v_lshlrev_b32_e32 v2, 3, v2
	v_and_b32_e32 v8, 24, v2
	v_lshrrev_b32_e32 v14, 2, v0
	v_mul_u32_u24_e32 v3, 0xc00, v14
	v_or_b32_e32 v2, v3, v8
	v_lshlrev_b32_e32 v2, 1, v2
	v_mov_b32_e32 v3, 0
	v_readfirstlane_b32 s41, v79
	v_readfirstlane_b32 s30, v45
	s_waitcnt lgkmcnt(0)
	s_add_u32 s26, s26, s28
	s_addc_u32 s27, s27, 0
	v_lshl_add_u64 v[4:5], s[26:27], 0, v[2:3]
	v_add_u32_e32 v2, 0x1000, v2
	v_lshl_add_u64 v[6:7], s[26:27], 0, v[2:3]
	v_bfe_u32 v9, v0, 2, 6
	v_add_u32_e32 v9, s39, v9
	v_lshlrev_b32_e32 v9, 12, v9
	v_lshl_or_b32 v9, v78, 11, v9
	v_lshl_or_b32 v2, v8, 1, v9
	v_lshl_add_u64 v[8:9], s[24:25], 0, v[2:3]
	s_add_i32 s28, s39, -1
	s_max_i32 s28, s28, 0
	s_lshl_b32 s28, s28, 12
	v_and_b32_e32 v2, 0xff, v0
	v_lshlrev_b32_e32 v2, 4, v2
	v_add_u32_e32 v2, s28, v2
	v_lshl_add_u64 v[10:11], s[24:25], 0, v[2:3]
	s_bfe_u32 s31, s30, 0x10001
	s_lshl_b32 s31, s31, 12
	s_and_b32 s34, s30, 1
	s_lshl_b32 s34, s34, 10
	s_or_b32 s31, s31, s34
	s_bfe_u32 s34, s30, 0x10002
	s_lshl_b32 s34, s34, 11
	s_or_b32 s31, s31, s34
	s_add_u32 s40, s31, 0x4000
	s_and_b32 s34, s41, 0xc00
	s_add_u32 s34, s34, 0x6000
	s_mov_b32 m0, s34
	s_add_u32 s35, s41, 0x2000
	global_load_lds_dwordx4 v[10:11], off
	s_mov_b32 m0, s41
	s_mov_b64 s[26:27], 0x80
	global_load_lds_dwordx4 v[4:5], off
	s_mov_b32 m0, s35
	s_mov_b64 s[28:29], 0xc0
	global_load_lds_dwordx4 v[6:7], off
	s_mov_b32 m0, s40
	s_nop 0
	global_load_lds_dwordx4 v[8:9], off
	s_add_u32 m0, s41, 0x8000
	v_lshl_add_u64 v[12:13], v[4:5], 0, 64
	global_load_lds_dwordx4 v[12:13], off
	s_add_u32 m0, s35, 0x8000
	v_lshl_add_u64 v[12:13], v[6:7], 0, 64
	global_load_lds_dwordx4 v[12:13], off
	s_add_u32 m0, s40, 0x8000
	v_lshl_add_u64 v[12:13], v[8:9], 0, 64
	global_load_lds_dwordx4 v[12:13], off
	s_add_u32 m0, s41, 0x10000
	v_lshl_add_u64 v[12:13], v[4:5], 0, s[26:27]
	global_load_lds_dwordx4 v[12:13], off
	s_add_u32 m0, s35, 0x10000
	v_lshl_add_u64 v[12:13], v[6:7], 0, s[26:27]
	global_load_lds_dwordx4 v[12:13], off
	s_add_u32 m0, s40, 0x10000
	v_lshl_add_u64 v[12:13], v[8:9], 0, s[26:27]
	global_load_lds_dwordx4 v[12:13], off
	s_add_u32 m0, s41, 0x18000
	v_lshl_add_u64 v[12:13], v[4:5], 0, s[28:29]
	global_load_lds_dwordx4 v[12:13], off
	s_add_u32 m0, s35, 0x18000
	v_lshl_add_u64 v[12:13], v[6:7], 0, s[28:29]
	global_load_lds_dwordx4 v[12:13], off
	s_add_u32 m0, s40, 0x18000
	v_lshl_add_u64 v[12:13], v[8:9], 0, s[28:29]
	global_load_lds_dwordx4 v[12:13], off
	s_mov_b64 s[26:27], 0x100
	v_lshl_add_u64 v[36:37], v[8:9], 0, s[26:27]
	v_lshl_add_u64 v[38:39], v[6:7], 0, s[26:27]
	v_lshl_add_u64 v[40:41], v[4:5], 0, s[26:27]
	s_mov_b64 s[26:27], 0
	v_lshlrev_b32_e32 v48, 6, v78
	v_and_b32_e32 v47, 32, v14
	v_and_b32_e32 v49, 32, v43
	v_and_b32_e32 v46, 63, v0
	v_or_b32_e32 v2, v48, v42
	v_or_b32_e32 v12, v2, v47
	v_lshlrev_b32_e32 v50, 6, v12
	v_sub_u32_e32 v13, 0, v14
	v_bitop3_b32 v13, v13, v1, 3 bitop3:0x6c
	v_lshlrev_b32_e32 v52, 4, v13
	v_cmp_eq_u32_e32 vcc, 0, v78
	s_and_b64 s[34:35], vcc, s[4:5]
	v_cndmask_b32_e64 v88, 0, 1, s[34:35]
	v_add_u32_e32 v89, v49, v42
	v_sub_u32_e32 v89, v89, v88
	v_cmp_eq_u32_e64 s[42:43], -1, v89
	v_and_b32_e32 v90, 32, v89
	v_lshlrev_b32_e32 v90, 7, v90
	v_and_b32_e32 v91, 31, v89
	v_lshl_or_b32 v90, v91, 6, v90
	v_ashrrev_i32_e32 v91, 2, v89
	v_sub_u32_e32 v91, 0, v91
	v_xor_b32_e32 v91, v91, v1
	v_and_b32_e32 v91, 3, v91
	v_lshl_or_b32 v92, v91, 4, v90
	v_add_u32_e32 v89, 16, v89
	v_and_b32_e32 v90, 32, v89
	v_lshlrev_b32_e32 v90, 7, v90
	v_and_b32_e32 v94, 31, v89
	v_lshl_or_b32 v90, v94, 6, v90
	v_lshl_or_b32 v93, v91, 4, v90
	v_lshlrev_b32_e32 v95, 4, v1
	v_add_u32_e32 v95, 0x2000, v95
	s_mov_b32 s37, 4
	s_mov_b32 s36, 0
	s_mov_b32 s38, 0
	v_mov_b32_e32 v2, v3
	v_mov_b32_e32 v4, v3
	v_mov_b32_e32 v5, v3
	v_mov_b32_e32 v6, v3
	v_mov_b32_e32 v7, v3
	v_mov_b32_e32 v8, v3
	v_mov_b32_e32 v9, v3
	v_mov_b32_e32 v10, v3
	v_mov_b32_e32 v11, v3
	v_mov_b32_e32 v12, v3
	v_mov_b32_e32 v13, v3
	v_mov_b32_e32 v14, v3
	v_mov_b32_e32 v15, v3
	v_mov_b32_e32 v16, v3
	v_mov_b32_e32 v17, v3
	v_mov_b32_e32 v18, v3
	v_mov_b32_e32 v19, v3
	v_mov_b32_e32 v20, v3
	v_mov_b32_e32 v21, v3
	v_mov_b32_e32 v22, v3
	v_mov_b32_e32 v23, v3
	v_mov_b32_e32 v24, v3
	v_mov_b32_e32 v25, v3
	v_mov_b32_e32 v26, v3
	v_mov_b32_e32 v27, v3
	v_mov_b32_e32 v28, v3
	v_mov_b32_e32 v29, v3
	v_mov_b32_e32 v30, v3
	v_mov_b32_e32 v31, v3
	v_mov_b32_e32 v32, v3
	v_mov_b32_e32 v33, v3
	s_branch .LBB1_3
.LBB1_2:
	s_lshl_b32 s28, s38, 15
	v_or_b32_e32 v53, s28, v50
	v_add_u32_e32 v88, s28, v92
	v_add_u32_e32 v53, v53, v52
	v_add_u32_e32 v89, s28, v93
	v_cndmask_b32_e64 v88, v88, v95, s[42:43]
	ds_read_b128 v[54:57], v53
	ds_read_b128 v[58:61], v88 offset:16384
	ds_read_b128 v[62:65], v53 offset:1024
	ds_read_b128 v[66:69], v89 offset:16384
	ds_read_b128 v[70:73], v88 offset:18432
	ds_read_b128 v[74:77], v89 offset:18432
	ds_read_b128 v[80:83], v53 offset:8192
	ds_read_b128 v[84:87], v53 offset:9216
	v_add_u32_e32 v95, 64, v95
	s_cmp_gt_u32 s36, 27
	s_cbranch_scc1 .Lpl_noissue
	s_lshl_b32 s28, s37, 15
	s_add_u32 s29, s28, s41
	s_mov_b32 m0, s29
	v_lshl_add_u64 v[96:97], v[40:41], 0, s[26:27]
	global_load_lds_dwordx4 v[96:97], off
	s_add_u32 m0, s29, 0x2000
	v_lshl_add_u64 v[96:97], v[38:39], 0, s[26:27]
	global_load_lds_dwordx4 v[96:97], off
	s_add_u32 m0, s28, s40
	v_lshl_add_u64 v[96:97], v[36:37], 0, s[26:27]
	global_load_lds_dwordx4 v[96:97], off
	.Lpl_noissue:
	s_waitcnt lgkmcnt(0)
	v_mfma_f32_16x16x32_f16 v[14:17], v[62:65], v[58:61], v[14:17]
	s_add_i32 s28, s38, 1
	s_cmp_lg_u32 s38, 4
	s_cselect_b32 s38, s28, 0
	v_mfma_f32_16x16x32_f16 v[30:33], v[54:57], v[58:61], v[30:33]
	s_add_i32 s28, s37, 1
	s_cmp_lg_u32 s37, 4
	s_cselect_b32 s37, s28, 0
	v_mfma_f32_16x16x32_f16 v[22:25], v[54:57], v[66:69], v[22:25]
	s_add_i32 s36, s36, 1
	s_add_u32 s26, s26, 64
	v_mfma_f32_16x16x32_f16 v[6:9], v[62:65], v[66:69], v[6:9]
	s_addc_u32 s27, s27, 0
	s_cmpk_lg_i32 s26, 0x800
	v_mfma_f32_16x16x32_f16 v[26:29], v[54:57], v[70:73], v[26:29]
	v_mfma_f32_16x16x32_f16 v[30:33], v[80:83], v[58:61], v[30:33]
	v_mfma_f32_16x16x32_f16 v[22:25], v[80:83], v[66:69], v[22:25]
	v_mfma_f32_16x16x32_f16 v[18:21], v[54:57], v[74:77], v[18:21]
	v_mfma_f32_16x16x32_f16 v[14:17], v[84:87], v[58:61], v[14:17]
	v_mfma_f32_16x16x32_f16 v[10:13], v[62:65], v[70:73], v[10:13]
	v_mfma_f32_16x16x32_f16 v[6:9], v[84:87], v[66:69], v[6:9]
	v_mfma_f32_16x16x32_f16 v[2:5], v[62:65], v[74:77], v[2:5]
	s_cbranch_scc0 .LBB1_19
.LBB1_3:
	s_cmp_gt_u32 s36, 28
	s_cbranch_scc1 .Lpl_tail_wait
	s_waitcnt vmcnt(9)
.LBB1_12:
	s_barrier
	s_branch .LBB1_2
.Lpl_tail_wait:
	s_cmp_eq_u32 s36, 29
	s_cbranch_scc0 .Lpl_tail_30
	s_waitcnt vmcnt(6)
	s_branch .LBB1_12
.Lpl_tail_30:
	s_cmp_eq_u32 s36, 30
	s_cbranch_scc0 .Lpl_tail_31
	s_waitcnt vmcnt(3)
	s_branch .LBB1_12
.Lpl_tail_31:
	s_waitcnt vmcnt(0)
	s_branch .LBB1_12

.LBB1_32:
	s_and_b64 vcc, exec, s[4:5]
	s_cbranch_vccz .LBB1_107
	s_and_b32 s4, s2, 3
	s_waitcnt lgkmcnt(0)
	s_mul_i32 s20, s4, 6
	s_mul_hi_i32 s4, s3, 0x2aaaaaab
	s_lshr_b32 s5, s4, 31
	s_add_i32 s21, s4, s5
	s_mul_i32 s4, s21, 6
	s_sub_i32 s3, s3, s4
	s_and_b32 s2, s2, 4
	s_add_i32 s20, s20, s3
	s_add_i32 s21, s21, s2
	s_load_dwordx2 s[0:1], s[0:1], 0x0
	s_lshl_b32 s4, s20, 7
	s_lshl_b32 s6, s21, 8
	s_ashr_i32 s5, s4, 31
	s_ashr_i32 s7, s6, 31
	v_xor_b32_e32 v2, v44, v0
	s_lshl_b64 s[2:3], s[4:5], 11
	s_lshl_b64 s[18:19], s[6:7], 12
	v_lshlrev_b32_e32 v120, 6, v78
	v_add_u32_e32 v120, s4, v120
	s_cmp_lt_i32 s20, 16
	s_cbranch_scc0 .Lqk_bias_swp
	v_lshl_add_u32 v120, v1, 2, v120
	v_lshlrev_b32_e32 v120, 2, v120
	global_load_dwordx4 v[128:131], v120, s[8:9]
	global_load_dwordx4 v[132:135], v120, s[8:9] offset:64
	global_load_dwordx4 v[136:139], v120, s[8:9] offset:128
	global_load_dwordx4 v[140:143], v120, s[8:9] offset:192
	s_branch .Lqk_bias_done
.Lqk_bias_swp:
	v_add_u32_e32 v120, v120, v42
	v_lshlrev_b32_e32 v120, 2, v120
	global_load_dword v128, v120, s[8:9]
	global_load_dword v129, v120, s[8:9] offset:64
	global_load_dword v130, v120, s[8:9] offset:128
	global_load_dword v131, v120, s[8:9] offset:192
.Lqk_bias_done:
	v_lshlrev_b32_e32 v5, 7, v0
	v_lshlrev_b32_e32 v2, 3, v2
	s_mov_b32 s7, 0x1fc00
	v_mov_b32_e32 v6, 0x10000
	s_add_u32 s16, s24, s18
	v_and_b32_e32 v3, 56, v2
	v_and_b32_e32 v4, 0xfc00, v5
	v_bitop3_b32 v5, v5, s7, v6 bitop3:0xc8
	v_lshlrev_b32_e32 v8, 8, v0
	s_mov_b32 s7, 0x3f800
	v_mov_b32_e32 v7, 0x20000
	s_addc_u32 s17, s25, s19
	v_or_b32_e32 v2, v4, v3
	v_bitop3_b32 v7, v8, s7, v7 bitop3:0xc8
	s_mov_b32 s7, 0x7f800
	v_mov_b32_e32 v11, 0x60000
	s_waitcnt lgkmcnt(0)
	s_add_u32 s22, s0, s2
	v_and_b32_e32 v6, 0x1f800, v8
	v_bitop3_b32 v8, v8, s7, v11 bitop3:0xc8
	v_lshlrev_b32_e32 v12, 1, v2
	v_mov_b32_e32 v2, 0
	v_readfirstlane_b32 s7, v79
	v_or_b32_e32 v9, v5, v3
	s_addc_u32 s23, s1, s3
	v_mov_b32_e32 v13, v2
	s_mov_b32 m0, s7
	v_lshl_add_u64 v[14:15], s[22:23], 0, v[12:13]
	global_load_lds_dwordx4 v12, s[22:23]
	v_lshlrev_b32_e32 v12, 1, v9
	v_or_b32_e32 v9, 0x2000, v79
	v_or_b32_e32 v10, v6, v3
	v_readfirstlane_b32 s7, v9
	v_or_b32_e32 v9, 0x4000, v79
	s_mov_b32 m0, s7
	v_readfirstlane_b32 s7, v9
	v_or_b32_e32 v9, 0x6000, v79
	v_or_b32_e32 v18, v7, v3
	v_lshlrev_b32_e32 v10, 1, v10
	global_load_lds_dwordx4 v12, s[22:23]
	s_mov_b32 m0, s7
	v_readfirstlane_b32 s7, v9
	v_or_b32_e32 v9, 0x8000, v79
	v_mov_b32_e32 v11, v2
	global_load_lds_dwordx4 v10, s[16:17]
	v_lshlrev_b32_e32 v18, 1, v18
	s_mov_b32 m0, s7
	v_readfirstlane_b32 s7, v9
	v_or_b32_e32 v9, 0xa000, v79
	v_or_b32_e32 v22, v8, v3
	v_lshl_add_u64 v[16:17], s[22:23], 0, v[12:13]
	v_lshl_add_u64 v[12:13], s[16:17], 0, v[10:11]
	v_mov_b32_e32 v19, v2
	global_load_lds_dwordx4 v18, s[16:17]
	v_or_b32_e32 v10, 0x80000, v10
	s_mov_b32 m0, s7
	v_readfirstlane_b32 s7, v9
	v_lshl_add_u64 v[20:21], s[16:17], 0, v[18:19]
	v_lshl_add_u64 v[18:19], s[16:17], 0, v[10:11]
	global_load_lds_dwordx4 v10, s[16:17]
	v_lshlrev_b32_e32 v10, 1, v22
	s_mov_b32 m0, s7
	v_or_b32_e32 v9, 0xc000, v79
	v_lshl_add_u64 v[22:23], s[16:17], 0, v[10:11]
	global_load_lds_dwordx4 v10, s[16:17]
	s_mov_b64 s[16:17], 0x80
	v_readfirstlane_b32 s7, v9
	v_or_b32_e32 v9, 0xe000, v79
	v_lshl_add_u64 v[10:11], v[14:15], 0, s[16:17]
	s_mov_b32 m0, s7
	v_readfirstlane_b32 s7, v9
	v_or_b32_e32 v9, 0x10000, v79
	global_load_lds_dwordx4 v[10:11], off
	v_lshl_add_u64 v[10:11], v[16:17], 0, s[16:17]
	s_mov_b32 m0, s7
	v_readfirstlane_b32 s7, v9
	v_or_b32_e32 v9, 0x12000, v79
	global_load_lds_dwordx4 v[10:11], off
	v_lshl_add_u64 v[10:11], v[12:13], 0, s[16:17]
	s_mov_b32 m0, s7
	v_readfirstlane_b32 s7, v9
	v_or_b32_e32 v9, 0x14000, v79
	global_load_lds_dwordx4 v[10:11], off
	v_lshl_add_u64 v[10:11], v[20:21], 0, s[16:17]
	s_mov_b32 m0, s7
	v_readfirstlane_b32 s7, v9
	v_or_b32_e32 v9, 0x16000, v79
	global_load_lds_dwordx4 v[10:11], off
	v_lshl_add_u64 v[10:11], v[18:19], 0, s[16:17]
	s_mov_b32 m0, s7
	v_readfirstlane_b32 s7, v9
	global_load_lds_dwordx4 v[10:11], off
	v_lshl_add_u64 v[10:11], v[22:23], 0, s[16:17]
	s_mov_b32 m0, s7
	s_nop 0
	global_load_lds_dwordx4 v[10:11], off
	s_waitcnt vmcnt(6)
	s_barrier
	s_mov_b32 s7, 0
	v_cmp_ne_u32_e32 vcc, 0, v78
	s_and_saveexec_b64 s[16:17], vcc
	s_cbranch_execz .LBB1_35
	s_barrier

.LBB1_39:
	s_or_b64 exec, exec, s[0:1]
	s_barrier
	v_and_b32_e32 v66, 15, v0
	v_bfe_u32 v67, v0, 6, 2
	v_and_b32_e32 v68, 7, v66
	v_lshlrev_b32_e32 v68, 1, v68
	v_lshlrev_b32_e32 v70, 15, v78
	s_cmp_lt_i32 s20, 16
	s_cbranch_scc0 .Lqk_epi_swp
	s_mov_b32 s0, 1.0
	s_cmp_lt_i32 s20, 8
	s_cselect_b32 s0, 0x3e38aa3b, s0
	v_xor_b32_e32 v69, v1, v68
	v_lshl_or_b32 v70, v67, 13, v70
	v_lshl_or_b32 v70, v66, 7, v70
	v_xor_b32_e32 v71, 0, v69
	v_lshl_add_u32 v71, v71, 3, v70
	v_pk_add_f32 v[72:73], v[62:63], v[128:129]
	v_pk_add_f32 v[74:75], v[64:65], v[130:131]
	v_pk_mul_f32 v[72:73], v[72:73], s[0:1] op_sel_hi:[1,0]
	v_pk_mul_f32 v[74:75], v[74:75], s[0:1] op_sel_hi:[1,0]
	v_cvt_pk_f16_f32 v72, v72, v73
	v_cvt_pk_f16_f32 v73, v74, v75
	ds_write_b64 v71, v[72:73]
	v_pk_add_f32 v[80:81], v[58:59], v[128:129]
	v_pk_add_f32 v[82:83], v[60:61], v[130:131]
	v_pk_mul_f32 v[80:81], v[80:81], s[0:1] op_sel_hi:[1,0]
	v_pk_mul_f32 v[82:83], v[82:83], s[0:1] op_sel_hi:[1,0]
	v_cvt_pk_f16_f32 v80, v80, v81
	v_cvt_pk_f16_f32 v81, v82, v83
	ds_write_b64 v71, v[80:81] offset:2048
	v_pk_add_f32 v[72:73], v[54:55], v[128:129]
	v_pk_add_f32 v[74:75], v[56:57], v[130:131]
	v_pk_mul_f32 v[72:73], v[72:73], s[0:1] op_sel_hi:[1,0]
	v_pk_mul_f32 v[74:75], v[74:75], s[0:1] op_sel_hi:[1,0]
	v_cvt_pk_f16_f32 v72, v72, v73
	v_cvt_pk_f16_f32 v73, v74, v75
	ds_write_b64 v71, v[72:73] offset:4096
	v_pk_add_f32 v[80:81], v[50:51], v[128:129]
	v_pk_add_f32 v[82:83], v[52:53], v[130:131]
	v_pk_mul_f32 v[80:81], v[80:81], s[0:1] op_sel_hi:[1,0]
	v_pk_mul_f32 v[82:83], v[82:83], s[0:1] op_sel_hi:[1,0]
	v_cvt_pk_f16_f32 v80, v80, v81
	v_cvt_pk_f16_f32 v81, v82, v83
	ds_write_b64 v71, v[80:81] offset:6144
	v_xor_b32_e32 v71, 4, v69
	v_lshl_add_u32 v71, v71, 3, v70
	v_pk_add_f32 v[72:73], v[46:47], v[132:133]
	v_pk_add_f32 v[74:75], v[48:49], v[134:135]
	v_pk_mul_f32 v[72:73], v[72:73], s[0:1] op_sel_hi:[1,0]
	v_pk_mul_f32 v[74:75], v[74:75], s[0:1] op_sel_hi:[1,0]
	v_cvt_pk_f16_f32 v72, v72, v73
	v_cvt_pk_f16_f32 v73, v74, v75
	ds_write_b64 v71, v[72:73]
	v_pk_add_f32 v[80:81], v[42:43], v[132:133]
	v_pk_add_f32 v[82:83], v[44:45], v[134:135]
	v_pk_mul_f32 v[80:81], v[80:81], s[0:1] op_sel_hi:[1,0]
	v_pk_mul_f32 v[82:83], v[82:83], s[0:1] op_sel_hi:[1,0]
	v_cvt_pk_f16_f32 v80, v80, v81
	v_cvt_pk_f16_f32 v81, v82, v83
	ds_write_b64 v71, v[80:81] offset:2048
	v_pk_add_f32 v[72:73], v[38:39], v[132:133]
	v_pk_add_f32 v[74:75], v[40:41], v[134:135]
	v_pk_mul_f32 v[72:73], v[72:73], s[0:1] op_sel_hi:[1,0]
	v_pk_mul_f32 v[74:75], v[74:75], s[0:1] op_sel_hi:[1,0]
	v_cvt_pk_f16_f32 v72, v72, v73
	v_cvt_pk_f16_f32 v73, v74, v75
	ds_write_b64 v71, v[72:73] offset:4096
	v_pk_add_f32 v[80:81], v[34:35], v[132:133]
	v_pk_add_f32 v[82:83], v[36:37], v[134:135]
	v_pk_mul_f32 v[80:81], v[80:81], s[0:1] op_sel_hi:[1,0]
	v_pk_mul_f32 v[82:83], v[82:83], s[0:1] op_sel_hi:[1,0]
	v_cvt_pk_f16_f32 v80, v80, v81
	v_cvt_pk_f16_f32 v81, v82, v83
	ds_write_b64 v71, v[80:81] offset:6144
	v_xor_b32_e32 v71, 8, v69
	v_lshl_add_u32 v71, v71, 3, v70
	v_pk_add_f32 v[72:73], v[30:31], v[136:137]
	v_pk_add_f32 v[74:75], v[32:33], v[138:139]
	v_pk_mul_f32 v[72:73], v[72:73], s[0:1] op_sel_hi:[1,0]
	v_pk_mul_f32 v[74:75], v[74:75], s[0:1] op_sel_hi:[1,0]
	v_cvt_pk_f16_f32 v72, v72, v73
	v_cvt_pk_f16_f32 v73, v74, v75
	ds_write_b64 v71, v[72:73]
	v_pk_add_f32 v[80:81], v[26:27], v[136:137]
	v_pk_add_f32 v[82:83], v[28:29], v[138:139]
	v_pk_mul_f32 v[80:81], v[80:81], s[0:1] op_sel_hi:[1,0]
	v_pk_mul_f32 v[82:83], v[82:83], s[0:1] op_sel_hi:[1,0]
	v_cvt_pk_f16_f32 v80, v80, v81
	v_cvt_pk_f16_f32 v81, v82, v83
	ds_write_b64 v71, v[80:81] offset:2048
	v_pk_add_f32 v[72:73], v[22:23], v[136:137]
	v_pk_add_f32 v[74:75], v[24:25], v[138:139]
	v_pk_mul_f32 v[72:73], v[72:73], s[0:1] op_sel_hi:[1,0]
	v_pk_mul_f32 v[74:75], v[74:75], s[0:1] op_sel_hi:[1,0]
	v_cvt_pk_f16_f32 v72, v72, v73
	v_cvt_pk_f16_f32 v73, v74, v75
	ds_write_b64 v71, v[72:73] offset:4096
	v_pk_add_f32 v[80:81], v[18:19], v[136:137]
	v_pk_add_f32 v[82:83], v[20:21], v[138:139]
	v_pk_mul_f32 v[80:81], v[80:81], s[0:1] op_sel_hi:[1,0]
	v_pk_mul_f32 v[82:83], v[82:83], s[0:1] op_sel_hi:[1,0]
	v_cvt_pk_f16_f32 v80, v80, v81
	v_cvt_pk_f16_f32 v81, v82, v83
	ds_write_b64 v71, v[80:81] offset:6144
	v_xor_b32_e32 v71, 12, v69
	v_lshl_add_u32 v71, v71, 3, v70
	v_pk_add_f32 v[72:73], v[14:15], v[140:141]
	v_pk_add_f32 v[74:75], v[16:17], v[142:143]
	v_pk_mul_f32 v[72:73], v[72:73], s[0:1] op_sel_hi:[1,0]
	v_pk_mul_f32 v[74:75], v[74:75], s[0:1] op_sel_hi:[1,0]
	v_cvt_pk_f16_f32 v72, v72, v73
	v_cvt_pk_f16_f32 v73, v74, v75
	ds_write_b64 v71, v[72:73]
	v_pk_add_f32 v[80:81], v[10:11], v[140:141]
	v_pk_add_f32 v[82:83], v[12:13], v[142:143]
	v_pk_mul_f32 v[80:81], v[80:81], s[0:1] op_sel_hi:[1,0]
	v_pk_mul_f32 v[82:83], v[82:83], s[0:1] op_sel_hi:[1,0]
	v_cvt_pk_f16_f32 v80, v80, v81
	v_cvt_pk_f16_f32 v81, v82, v83
	ds_write_b64 v71, v[80:81] offset:2048
	v_pk_add_f32 v[72:73], v[6:7], v[140:141]
	v_pk_add_f32 v[74:75], v[8:9], v[142:143]
	v_pk_mul_f32 v[72:73], v[72:73], s[0:1] op_sel_hi:[1,0]
	v_pk_mul_f32 v[74:75], v[74:75], s[0:1] op_sel_hi:[1,0]
	v_cvt_pk_f16_f32 v72, v72, v73
	v_cvt_pk_f16_f32 v73, v74, v75
	ds_write_b64 v71, v[72:73] offset:4096
	v_pk_add_f32 v[80:81], v[2:3], v[140:141]
	v_pk_add_f32 v[82:83], v[4:5], v[142:143]
	v_pk_mul_f32 v[80:81], v[80:81], s[0:1] op_sel_hi:[1,0]
	v_pk_mul_f32 v[82:83], v[82:83], s[0:1] op_sel_hi:[1,0]
	v_cvt_pk_f16_f32 v80, v80, v81
	v_cvt_pk_f16_f32 v81, v82, v83
	ds_write_b64 v71, v[80:81] offset:6144
	s_branch .Lqk_epi_join
.Lqk_epi_swp:
	v_lshlrev_b32_e32 v69, 1, v1
	v_xor_b32_e32 v69, v69, v68
	v_lshl_or_b32 v70, v66, 9, v70
	v_lshl_or_b32 v70, v67, 7, v70
	v_xor_b32_e32 v71, 0, v69
	v_lshl_add_u32 v71, v71, 3, v70
	v_add_f32_e32 v72, v62, v128
	v_add_f32_e32 v73, v63, v128
	v_add_f32_e32 v74, v64, v128
	v_add_f32_e32 v75, v65, v128
	v_cvt_pk_f16_f32 v72, v72, v73
	v_cvt_pk_f16_f32 v73, v74, v75
	ds_write_b64 v71, v[72:73]
	v_add_f32_e32 v80, v58, v129
	v_add_f32_e32 v81, v59, v129
	v_add_f32_e32 v82, v60, v129
	v_add_f32_e32 v83, v61, v129
	v_cvt_pk_f16_f32 v80, v80, v81
	v_cvt_pk_f16_f32 v81, v82, v83
	ds_write_b64 v71, v[80:81] offset:8192
	v_add_f32_e32 v72, v54, v130
	v_add_f32_e32 v73, v55, v130
	v_add_f32_e32 v74, v56, v130
	v_add_f32_e32 v75, v57, v130
	v_cvt_pk_f16_f32 v72, v72, v73
	v_cvt_pk_f16_f32 v73, v74, v75
	ds_write_b64 v71, v[72:73] offset:16384
	v_add_f32_e32 v80, v50, v131
	v_add_f32_e32 v81, v51, v131
	v_add_f32_e32 v82, v52, v131
	v_add_f32_e32 v83, v53, v131
	v_cvt_pk_f16_f32 v80, v80, v81
	v_cvt_pk_f16_f32 v81, v82, v83
	ds_write_b64 v71, v[80:81] offset:24576
	v_xor_b32_e32 v71, 1, v69
	v_lshl_add_u32 v71, v71, 3, v70
	v_add_f32_e32 v72, v46, v128
	v_add_f32_e32 v73, v47, v128
	v_add_f32_e32 v74, v48, v128
	v_add_f32_e32 v75, v49, v128
	v_cvt_pk_f16_f32 v72, v72, v73
	v_cvt_pk_f16_f32 v73, v74, v75
	ds_write_b64 v71, v[72:73]
	v_add_f32_e32 v80, v42, v129
	v_add_f32_e32 v81, v43, v129
	v_add_f32_e32 v82, v44, v129
	v_add_f32_e32 v83, v45, v129
	v_cvt_pk_f16_f32 v80, v80, v81
	v_cvt_pk_f16_f32 v81, v82, v83
	ds_write_b64 v71, v[80:81] offset:8192
	v_add_f32_e32 v72, v38, v130
	v_add_f32_e32 v73, v39, v130
	v_add_f32_e32 v74, v40, v130
	v_add_f32_e32 v75, v41, v130
	v_cvt_pk_f16_f32 v72, v72, v73
	v_cvt_pk_f16_f32 v73, v74, v75
	ds_write_b64 v71, v[72:73] offset:16384
	v_add_f32_e32 v80, v34, v131
	v_add_f32_e32 v81, v35, v131
	v_add_f32_e32 v82, v36, v131
	v_add_f32_e32 v83, v37, v131
	v_cvt_pk_f16_f32 v80, v80, v81
	v_cvt_pk_f16_f32 v81, v82, v83
	ds_write_b64 v71, v[80:81] offset:24576
	v_xor_b32_e32 v71, 8, v69
	v_lshl_add_u32 v71, v71, 3, v70
	v_add_f32_e32 v72, v30, v128
	v_add_f32_e32 v73, v31, v128
	v_add_f32_e32 v74, v32, v128
	v_add_f32_e32 v75, v33, v128
	v_cvt_pk_f16_f32 v72, v72, v73
	v_cvt_pk_f16_f32 v73, v74, v75
	ds_write_b64 v71, v[72:73]
	v_add_f32_e32 v80, v26, v129
	v_add_f32_e32 v81, v27, v129
	v_add_f32_e32 v82, v28, v129
	v_add_f32_e32 v83, v29, v129
	v_cvt_pk_f16_f32 v80, v80, v81
	v_cvt_pk_f16_f32 v81, v82, v83
	ds_write_b64 v71, v[80:81] offset:8192
	v_add_f32_e32 v72, v22, v130
	v_add_f32_e32 v73, v23, v130
	v_add_f32_e32 v74, v24, v130
	v_add_f32_e32 v75, v25, v130
	v_cvt_pk_f16_f32 v72, v72, v73
	v_cvt_pk_f16_f32 v73, v74, v75
	ds_write_b64 v71, v[72:73] offset:16384
	v_add_f32_e32 v80, v18, v131
	v_add_f32_e32 v81, v19, v131
	v_add_f32_e32 v82, v20, v131
	v_add_f32_e32 v83, v21, v131
	v_cvt_pk_f16_f32 v80, v80, v81
	v_cvt_pk_f16_f32 v81, v82, v83
	ds_write_b64 v71, v[80:81] offset:24576
	v_xor_b32_e32 v71, 9, v69
	v_lshl_add_u32 v71, v71, 3, v70
	v_add_f32_e32 v72, v14, v128
	v_add_f32_e32 v73, v15, v128
	v_add_f32_e32 v74, v16, v128
	v_add_f32_e32 v75, v17, v128
	v_cvt_pk_f16_f32 v72, v72, v73
	v_cvt_pk_f16_f32 v73, v74, v75
	ds_write_b64 v71, v[72:73]
	v_add_f32_e32 v80, v10, v129
	v_add_f32_e32 v81, v11, v129
	v_add_f32_e32 v82, v12, v129
	v_add_f32_e32 v83, v13, v129
	v_cvt_pk_f16_f32 v80, v80, v81
	v_cvt_pk_f16_f32 v81, v82, v83
	ds_write_b64 v71, v[80:81] offset:8192
	v_add_f32_e32 v72, v6, v130
	v_add_f32_e32 v73, v7, v130
	v_add_f32_e32 v74, v8, v130
	v_add_f32_e32 v75, v9, v130
	v_cvt_pk_f16_f32 v72, v72, v73
	v_cvt_pk_f16_f32 v73, v74, v75
	ds_write_b64 v71, v[72:73] offset:16384
	v_add_f32_e32 v80, v2, v131
	v_add_f32_e32 v81, v3, v131
	v_add_f32_e32 v82, v4, v131
	v_add_f32_e32 v83, v5, v131
	v_cvt_pk_f16_f32 v80, v80, v81
	v_cvt_pk_f16_f32 v81, v82, v83
	ds_write_b64 v71, v[80:81] offset:24576
.Lqk_epi_join:
	s_ashr_i32 s5, s21, 2
	s_and_b32 s6, s6, 0x300
	v_lshlrev_b32_e32 v1, 3, v0
	v_and_b32_e32 v1, 56, v1
	s_mov_b64 s[0:1], -1
	s_waitcnt vmcnt(0) lgkmcnt(0)
	s_barrier
	s_cmp_gt_i32 s20, 15
	s_cbranch_scc1 .LBB1_105
	s_cmp_gt_i32 s20, 7
	s_cselect_b32 s1, s13, s11
	s_cselect_b32 s0, s12, s10
	s_lshl_b32 s3, s20, 11
	s_lshl_b32 s2, s5, 14
	s_and_b32 s3, s3, 0x3800
	s_or_b32 s2, s2, s3
	v_lshrrev_b32_e32 v12, 3, v0
	s_or_b32 s2, s2, s6
	v_or_b32_e32 v6, s2, v12
	v_xor_b32_e32 v2, v12, v0
	v_ashrrev_i32_e32 v7, 31, v6
	v_lshlrev_b32_e32 v2, 4, v2
	v_lshlrev_b64 v[8:9], 7, v[6:7]
	v_and_b32_e32 v13, 0x70, v2
	v_lshl_add_u64 v[8:9], s[0:1], 0, v[8:9]
	v_lshlrev_b32_e32 v10, 1, v1
	v_mov_b32_e32 v11, 0
	v_or_b32_e32 v1, 0x200, v0
	v_lshl_or_b32 v14, v12, 7, v13
	v_lshl_add_u64 v[8:9], v[8:9], 0, v[10:11]
	v_lshrrev_b32_e32 v1, 3, v1
	ds_read_b128 v[2:5], v14
	s_waitcnt lgkmcnt(0)
	global_store_dwordx4 v[8:9], v[2:5], off nt
	s_nop 1
	v_or_b32_e32 v8, s2, v1
	v_xor_b32_e32 v2, v1, v0
	v_ashrrev_i32_e32 v9, 31, v8
	v_lshlrev_b32_e32 v2, 4, v2
	v_lshlrev_b64 v[8:9], 7, v[8:9]
	v_and_b32_e32 v2, 0x70, v2
	v_lshl_add_u64 v[8:9], s[0:1], 0, v[8:9]
	v_lshl_or_b32 v2, v1, 7, v2
	v_lshl_add_u64 v[8:9], v[8:9], 0, v[10:11]
	v_or_b32_e32 v1, 0x80, v12
	ds_read_b128 v[2:5], v2
	s_waitcnt lgkmcnt(0)
	global_store_dwordx4 v[8:9], v[2:5], off nt
	s_nop 1
	v_or_b32_e32 v8, s2, v1
	v_ashrrev_i32_e32 v9, 31, v8
	v_lshl_or_b32 v15, v1, 7, v13
	v_lshlrev_b64 v[12:13], 7, v[8:9]
	v_lshl_add_u64 v[12:13], s[0:1], 0, v[12:13]
	v_or_b32_e32 v1, 0x600, v0
	ds_read_b128 v[2:5], v15
	v_lshl_add_u64 v[12:13], v[12:13], 0, v[10:11]
	v_lshrrev_b32_e32 v1, 3, v1
	s_waitcnt lgkmcnt(0)
	global_store_dwordx4 v[12:13], v[2:5], off nt
	s_nop 1
	v_xor_b32_e32 v2, v1, v0
	v_or_b32_e32 v12, s2, v1
	v_lshlrev_b32_e32 v2, 4, v2
	v_ashrrev_i32_e32 v13, 31, v12
	v_and_b32_e32 v2, 0x70, v2
	v_lshlrev_b64 v[12:13], 7, v[12:13]
	v_or_b32_e32 v6, 0x400, v6
	v_lshl_or_b32 v2, v1, 7, v2
	v_lshl_add_u64 v[12:13], s[0:1], 0, v[12:13]
	v_ashrrev_i32_e32 v7, 31, v6
	ds_read_b128 v[2:5], v2
	v_lshl_add_u64 v[12:13], v[12:13], 0, v[10:11]
	s_waitcnt lgkmcnt(0)
	global_store_dwordx4 v[12:13], v[2:5], off nt
	s_nop 1
	v_lshlrev_b64 v[6:7], 7, v[6:7]
	ds_read_b128 v[2:5], v14 offset:32768
	v_lshl_add_u64 v[6:7], s[0:1], 0, v[6:7]
	v_or_b32_e32 v1, 0xa00, v0
	v_lshl_add_u64 v[6:7], v[6:7], 0, v[10:11]
	s_waitcnt lgkmcnt(0)
	global_store_dwordx4 v[6:7], v[2:5], off nt
	s_nop 1
	v_lshrrev_b32_e32 v2, 3, v1
	v_xor_b32_e32 v2, v2, v0
	v_lshlrev_b32_e32 v2, 4, v2
	v_bfe_u32 v1, v1, 3, 7
	v_and_b32_e32 v2, 0x70, v2
	v_lshl_or_b32 v2, v1, 7, v2
	v_or_b32_e32 v1, s2, v1
	v_or_b32_e32 v6, 0x400, v1
	v_ashrrev_i32_e32 v7, 31, v6
	v_lshlrev_b64 v[6:7], 7, v[6:7]
	v_lshl_add_u64 v[6:7], s[0:1], 0, v[6:7]
	v_lshl_add_u64 v[6:7], v[6:7], 0, v[10:11]
	ds_read_b128 v[2:5], v2 offset:32768
	s_waitcnt lgkmcnt(0)
	global_store_dwordx4 v[6:7], v[2:5], off nt
	s_nop 1
	v_or_b32_e32 v6, 0x400, v8
	v_ashrrev_i32_e32 v7, 31, v6
	v_lshlrev_b64 v[6:7], 7, v[6:7]
	ds_read_b128 v[2:5], v15 offset:32768
	v_lshl_add_u64 v[6:7], s[0:1], 0, v[6:7]
	v_or_b32_e32 v1, 0xe00, v0
	v_lshl_add_u64 v[6:7], v[6:7], 0, v[10:11]
	s_waitcnt lgkmcnt(0)
	global_store_dwordx4 v[6:7], v[2:5], off nt
	s_nop 1
	v_lshrrev_b32_e32 v2, 3, v1
	v_bfe_u32 v1, v1, 3, 8
	v_add_u32_e32 v1, s2, v1
	v_xor_b32_e32 v3, v2, v0
	v_add_u32_e32 v6, 0x400, v1
	v_lshlrev_b32_e32 v3, 4, v3
	v_ashrrev_i32_e32 v7, 31, v6
	v_and_b32_e32 v3, 0x70, v3
	v_lshlrev_b64 v[6:7], 7, v[6:7]
	v_lshl_or_b32 v2, v2, 7, v3
	v_lshl_add_u64 v[6:7], s[0:1], 0, v[6:7]
	ds_read_b128 v[2:5], v2
	v_lshl_add_u64 v[6:7], v[6:7], 0, v[10:11]
	s_waitcnt lgkmcnt(0)
	global_store_dwordx4 v[6:7], v[2:5], off nt
	s_nop 1
	s_mov_b64 s[0:1], 0

	.amdhsa_kernel _Z12gemm1_kernel6G1Args
		.amdhsa_group_segment_fixed_size 163840
		.amdhsa_private_segment_fixed_size 0
		.amdhsa_kernarg_size 88
		.amdhsa_user_sgpr_count 2
		.amdhsa_user_sgpr_dispatch_ptr 0
		.amdhsa_user_sgpr_queue_ptr 0
		.amdhsa_user_sgpr_kernarg_segment_ptr 1
		.amdhsa_user_sgpr_dispatch_id 0
		.amdhsa_user_sgpr_kernarg_preload_length 0
		.amdhsa_user_sgpr_kernarg_preload_offset 0
		.amdhsa_user_sgpr_private_segment_size 0
		.amdhsa_uses_dynamic_stack 0
		.amdhsa_enable_private_segment 0
		.amdhsa_system_sgpr_workgroup_id_x 1
		.amdhsa_system_sgpr_workgroup_id_y 0
		.amdhsa_system_sgpr_workgroup_id_z 0
		.amdhsa_system_sgpr_workgroup_info 0
		.amdhsa_system_vgpr_workitem_id 0
		.amdhsa_next_free_vgpr 169
		.amdhsa_next_free_sgpr 96
		.amdhsa_accum_offset 144
		.amdhsa_reserve_vcc 1
		.amdhsa_float_round_mode_32 0
		.amdhsa_float_round_mode_16_64 0
		.amdhsa_float_denorm_mode_32 3
		.amdhsa_float_denorm_mode_16_64 3
		.amdhsa_dx10_clamp 1
		.amdhsa_ieee_mode 1
		.amdhsa_fp16_overflow 0
		.amdhsa_tg_split 0
		.amdhsa_exception_fp_ieee_invalid_op 0
		.amdhsa_exception_fp_denorm_src 0
		.amdhsa_exception_fp_ieee_div_zero 0
		.amdhsa_exception_fp_ieee_overflow 0
		.amdhsa_exception_fp_ieee_underflow 0
		.amdhsa_exception_fp_ieee_inexact 0
		.amdhsa_exception_int_div_zero 0
	.end_amdhsa_kernel

amdhsa.kernels:
  - .agpr_count:     0
    .args:
      - .actual_access:  read_only
        .address_space:  global
        .offset:         0
        .size:           8
        .value_kind:     global_buffer
      - .actual_access:  read_only
        .address_space:  global
        .offset:         8
        .size:           8
        .value_kind:     global_buffer
      - .actual_access:  read_only
        .address_space:  global
        .offset:         16
        .size:           8
        .value_kind:     global_buffer
      - .actual_access:  read_only
        .address_space:  global
        .offset:         24
        .size:           8
        .value_kind:     global_buffer
      - .actual_access:  read_only
        .address_space:  global
        .offset:         32
        .size:           8
        .value_kind:     global_buffer
      - .actual_access:  read_only
        .address_space:  global
        .offset:         40
        .size:           8
        .value_kind:     global_buffer
      - .actual_access:  read_only
        .address_space:  global
        .offset:         48
        .size:           8
        .value_kind:     global_buffer
      - .address_space:  global
        .offset:         56
        .size:           8
        .value_kind:     global_buffer
      - .address_space:  global
        .offset:         64
        .size:           8
        .value_kind:     global_buffer
      - .actual_access:  read_only
        .address_space:  global
        .offset:         72
        .size:           8
        .value_kind:     global_buffer
      - .address_space:  global
        .offset:         80
        .size:           8
        .value_kind:     global_buffer
    .group_segment_fixed_size: 0
    .kernarg_segment_align: 8
    .kernarg_segment_size: 88
    .language:       OpenCL C
    .language_version:
      - 2
      - 0
    .max_flat_workgroup_size: 256
    .name:           _Z11prep_kernelPKfS0_S0_S0_S0_S0_S0_PDF16_S1_S1_S1_
    .private_segment_fixed_size: 0
    .sgpr_count:     23
    .sgpr_spill_count: 0
    .symbol:         _Z11prep_kernelPKfS0_S0_S0_S0_S0_S0_PDF16_S1_S1_S1_.kd
    .uniform_work_group_size: 1
    .uses_dynamic_stack: false
    .vgpr_count:     28
    .vgpr_spill_count: 0
    .wavefront_size: 64
  - .agpr_count:     0
    .args:
      - .offset:         0
        .size:           88
        .value_kind:     by_value
    .group_segment_fixed_size: 163840
    .kernarg_segment_align: 8
    .kernarg_segment_size: 88
    .language:       OpenCL C
    .language_version:
      - 2
      - 0
    .max_flat_workgroup_size: 512
    .name:           _Z12gemm1_kernel6G1Args
    .private_segment_fixed_size: 0
    .sgpr_count:     50
    .sgpr_spill_count: 0
    .symbol:         _Z12gemm1_kernel6G1Args.kd
    .uniform_work_group_size: 1
    .uses_dynamic_stack: false
    .vgpr_count:     144
    .vgpr_spill_count: 0
    .wavefront_size: 64
  - .agpr_count:     0
    .args:
      - .address_space:  global
        .offset:         0
        .size:           8
        .value_kind:     global_buffer
      - .address_space:  global
        .offset:         8
        .size:           8
        .value_kind:     global_buffer
      - .address_space:  global
        .offset:         16
        .size:           8
        .value_kind:     global_buffer
      - .actual_access:  read_only
        .address_space:  global
        .offset:         24
        .size:           8
        .value_kind:     global_buffer
      - .actual_access:  read_only
        .address_space:  global
        .offset:         32
        .size:           8
        .value_kind:     global_buffer
      - .actual_access:  read_only
        .address_space:  global
        .offset:         40
        .size:           8
        .value_kind:     global_buffer
      - .address_space:  global
        .offset:         48
        .size:           8
        .value_kind:     global_buffer
      - .actual_access:  read_only
        .address_space:  global
        .offset:         56
        .size:           8
        .value_kind:     global_buffer
      - .address_space:  global
        .offset:         64
        .size:           8
        .value_kind:     global_buffer
      - .actual_access:  read_only
        .address_space:  global
        .offset:         72
        .size:           8
        .value_kind:     global_buffer
      - .address_space:  global
        .offset:         80
        .size:           8
        .value_kind:     global_buffer
    .group_segment_fixed_size: 81920
    .kernarg_segment_align: 8
    .kernarg_segment_size: 88
    .language:       OpenCL C
    .language_version:
      - 2
      - 0
    .max_flat_workgroup_size: 512
    .name:           _Z11attn_kernelPKDF16_S0_S0_PKfS2_S2_S0_S2_PDF16_S2_S3_
    .private_segment_fixed_size: 0
    .sgpr_count:     62
    .sgpr_spill_count: 0
    .symbol:         _Z11attn_kernelPKDF16_S0_S0_PKfS2_S2_S0_S2_PDF16_S2_S3_.kd
    .uniform_work_group_size: 1
    .uses_dynamic_stack: false
    .vgpr_count:     126
    .vgpr_spill_count: 0
    .wavefront_size: 64
  - .agpr_count:     0
    .args:
      - .address_space:  global
        .offset:         0
        .size:           8
        .value_kind:     global_buffer
      - .address_space:  global
        .offset:         8
        .size:           8
        .value_kind:     global_buffer
      - .actual_access:  read_only
        .address_space:  global
        .offset:         16
        .size:           8
        .value_kind:     global_buffer
      - .actual_access:  write_only
        .address_space:  global
        .offset:         24
        .size:           8
        .value_kind:     global_buffer
    .group_segment_fixed_size: 122880
    .kernarg_segment_align: 8
    .kernarg_segment_size: 32
    .language:       OpenCL C
    .language_version:
      - 2
      - 0
    .max_flat_workgroup_size: 512
    .name:           _Z14outproj_kernelPKDF16_S0_PKfPf
    .private_segment_fixed_size: 0
    .sgpr_count:     30
    .sgpr_spill_count: 0
    .symbol:         _Z14outproj_kernelPKDF16_S0_PKfPf.kd
    .uniform_work_group_size: 1
    .uses_dynamic_stack: false
    .vgpr_count:     90
    .vgpr_spill_count: 0
    .wavefront_size: 64
